# v26 + grid barrier: non-leader workgroups poll the top-level generation word directly instead of the per-XCD generation (one hop fewer)
# speedup vs baseline: 1.0044x; 1.0002x over previous
; __device__ __forceinline__ unsigned xb_ld(unsigned* p)              { return __hip_atomic_load(p, __ATOMIC_RELAXED, __HIP_MEMORY_SCOPE_AGENT); }
; __device__ __forceinline__ unsigned xb_add(unsigned* p, unsigned v) { return __hip_atomic_fetch_add(p, v, __ATOMIC_RELAXED, __HIP_MEMORY_SCOPE_AGENT); }
; #define XB_SPIN(cond, bar) do { unsigned _sp = 0; while (cond) { __builtin_amdgcn_s_sleep(1); \
;     if ((++_sp & 255u) == 0u) { if (xb_ld(&(bar)[XB_TMO])) break; if (_sp > XB_SPIN_CAP) { atomicAdd(&(bar)[XB_TMO], 1u); break; } } } } while (0)
; __device__ __forceinline__ void xcd_barrier(const XcdBarrier& b) {
;     ...
;     if (threadIdx.x == 0) {
;         unsigned* bar = b.bar;
;         __builtin_amdgcn_s_waitcnt(0);
;         unsigned nloc = b.st[0], nx = b.st[1];
;         if (nloc == 0u) { xcd_barrier_complete(bar, b.x, nloc, nx); b.st[0] = nloc; b.st[1] = nx; }
;         const unsigned old = xb_add(&bar[XB_XSUB(b.x)], 1u);
;         const unsigned gen = old / nloc;
;         if (old + 1u == (gen + 1u) * nloc) {
;             __builtin_amdgcn_fence(__ATOMIC_RELEASE, "agent");
;             asm volatile("s_waitcnt vmcnt(0)" ::: "memory");
;             const unsigned og = xb_add(&bar[XB_TOP], 1u);
;             const unsigned tg = og / nx;
;             if (og + 1u == (tg + 1u) * nx) xb_add(&bar[XB_TOPGEN], 1u);
;             else XB_SPIN(xb_ld(&bar[XB_TOPGEN]) == tg, bar);
;             __builtin_amdgcn_fence(__ATOMIC_ACQUIRE, "agent");
;             xb_add(&bar[XB_XGEN(b.x)], 1u);
;             asm volatile("s_waitcnt vmcnt(0)" ::: "memory");
;         } else {
;             XB_SPIN(xb_ld(&bar[XB_XGEN(b.x)]) == gen, bar);
;             __builtin_amdgcn_fence(__ATOMIC_ACQUIRE, "agent");
;             asm volatile("s_waitcnt vmcnt(0)" ::: "memory");
;         }
.LBB0_108:
	s_lshl_b32 s20, s33, 6
	s_add_i32 s2, s20, 0x500
	s_mov_b32 s3, 0
	s_lshl_b64 s[0:1], s[2:3], 2
	s_add_u32 s0, s30, s0
	s_addc_u32 s1, s31, s1
	v_mov_b32_e32 v1, 1
	v_mov_b64_e32 v[6:7], s[0:1]
	flat_atomic_add v1, v[6:7], v1 sc0
	v_cvt_f32_u32_e32 v3, v4
	v_sub_u32_e32 v5, 0, v4
	v_rcp_iflag_f32_e32 v3, v3
	s_nop 0
	v_mul_f32_e32 v3, 0x4f7ffffe, v3
	v_cvt_u32_f32_e32 v3, v3
	v_mul_lo_u32 v5, v5, v3
	v_mul_hi_u32 v5, v3, v5
	v_add_u32_e32 v3, v3, v5
	s_waitcnt vmcnt(0) lgkmcnt(0)
	v_mul_hi_u32 v3, v1, v3
	v_mul_lo_u32 v5, v3, v4
	v_add_u32_e32 v6, 1, v1
	v_sub_u32_e32 v1, v1, v5
	v_add_u32_e32 v7, 1, v3
	v_cmp_ge_u32_e32 vcc, v1, v4
	v_sub_u32_e32 v5, v1, v4
	s_nop 0
	v_cndmask_b32_e32 v3, v3, v7, vcc
	v_cndmask_b32_e32 v1, v1, v5, vcc
	v_add_u32_e32 v5, 1, v3
	v_cmp_ge_u32_e32 vcc, v1, v4
	s_nop 1
	v_cndmask_b32_e32 v1, v3, v5, vcc
	v_mad_u64_u32 v[4:5], s[0:1], v4, v1, v[4:5]
	v_cmp_ne_u32_e32 vcc, v6, v4
	s_and_saveexec_b64 s[0:1], vcc
	s_xor_b64 s[0:1], exec, s[0:1]
	s_cbranch_execz .LBB0_121
	s_movk_i32 s2, 0xd40
	s_lshl_b64 s[2:3], s[2:3], 2
	s_add_u32 s4, s30, s2
	s_addc_u32 s5, s31, s3
	v_mov_b64_e32 v[2:3], s[4:5]
	flat_load_dword v2, v[2:3] sc1
	s_waitcnt vmcnt(0) lgkmcnt(0)
	v_cmp_eq_u32_e32 vcc, v2, v1
	s_and_saveexec_b64 s[2:3], vcc
	s_cbranch_execz .LBB0_120
	s_mov_b32 s21, 1
	s_mov_b64 s[6:7], 0
	s_branch .LBB0_112

; __device__ __forceinline__ unsigned xb_ld(unsigned* p)              { return __hip_atomic_load(p, __ATOMIC_RELAXED, __HIP_MEMORY_SCOPE_AGENT); }
; __device__ __forceinline__ unsigned xb_add(unsigned* p, unsigned v) { return __hip_atomic_fetch_add(p, v, __ATOMIC_RELAXED, __HIP_MEMORY_SCOPE_AGENT); }
; #define XB_SPIN(cond, bar) do { unsigned _sp = 0; while (cond) { __builtin_amdgcn_s_sleep(1); \
;     if ((++_sp & 255u) == 0u) { if (xb_ld(&(bar)[XB_TMO])) break; if (_sp > XB_SPIN_CAP) { atomicAdd(&(bar)[XB_TMO], 1u); break; } } } } while (0)
; __device__ __forceinline__ void xcd_barrier(const XcdBarrier& b) {
;     ...
;     if (threadIdx.x == 0) {
;         unsigned* bar = b.bar;
;         __builtin_amdgcn_s_waitcnt(0);
;         unsigned nloc = b.st[0], nx = b.st[1];
;         if (nloc == 0u) { xcd_barrier_complete(bar, b.x, nloc, nx); b.st[0] = nloc; b.st[1] = nx; }
;         const unsigned old = xb_add(&bar[XB_XSUB(b.x)], 1u);
;         const unsigned gen = old / nloc;
;         if (old + 1u == (gen + 1u) * nloc) {
;             __builtin_amdgcn_fence(__ATOMIC_RELEASE, "agent");
;             asm volatile("s_waitcnt vmcnt(0)" ::: "memory");
;             const unsigned og = xb_add(&bar[XB_TOP], 1u);
;             const unsigned tg = og / nx;
;             if (og + 1u == (tg + 1u) * nx) xb_add(&bar[XB_TOPGEN], 1u);
;             else XB_SPIN(xb_ld(&bar[XB_TOPGEN]) == tg, bar);
;             __builtin_amdgcn_fence(__ATOMIC_ACQUIRE, "agent");
;             xb_add(&bar[XB_XGEN(b.x)], 1u);
;             asm volatile("s_waitcnt vmcnt(0)" ::: "memory");
;         } else {
;             XB_SPIN(xb_ld(&bar[XB_XGEN(b.x)]) == gen, bar);
;             __builtin_amdgcn_fence(__ATOMIC_ACQUIRE, "agent");
;             asm volatile("s_waitcnt vmcnt(0)" ::: "memory");
;         }
.LBB0_615:
	s_lshl_b32 s1, s1, 6
	s_add_i32 s68, s1, 0x500
	s_lshl_b64 s[2:3], s[68:69], 2
	s_add_u32 s2, s34, s2
	s_addc_u32 s3, s35, s3
	v_mov_b64_e32 v[6:7], s[2:3]
	flat_atomic_add v6, v[6:7], v1 sc0
	v_cvt_f32_u32_e32 v5, v4
	v_sub_u32_e32 v7, 0, v4
	v_rcp_iflag_f32_e32 v5, v5
	s_nop 0
	v_mul_f32_e32 v5, 0x4f7ffffe, v5
	v_cvt_u32_f32_e32 v5, v5
	v_mul_lo_u32 v7, v7, v5
	v_mul_hi_u32 v7, v5, v7
	v_add_u32_e32 v5, v5, v7
	s_waitcnt vmcnt(0) lgkmcnt(0)
	v_mul_hi_u32 v5, v6, v5
	v_mul_lo_u32 v7, v5, v4
	v_sub_u32_e32 v7, v6, v7
	v_cmp_ge_u32_e32 vcc, v7, v4
	v_add_u32_e32 v8, 1, v5
	s_nop 0
	v_cndmask_b32_e32 v5, v5, v8, vcc
	v_sub_u32_e32 v8, v7, v4
	v_cndmask_b32_e32 v7, v7, v8, vcc
	v_cmp_ge_u32_e32 vcc, v7, v4
	v_add_u32_e32 v7, 1, v5
	v_add_u32_e32 v8, 1, v6
	v_cndmask_b32_e32 v5, v5, v7, vcc
	v_mad_u64_u32 v[6:7], s[2:3], v4, v5, v[4:5]
	v_cmp_ne_u32_e32 vcc, v8, v6
	s_and_saveexec_b64 s[2:3], vcc
	s_xor_b64 s[2:3], exec, s[2:3]
	s_cbranch_execz .LBB0_628
	s_movk_i32 s68, 0xd40
	s_lshl_b64 s[4:5], s[68:69], 2
	s_add_u32 s6, s34, s4
	s_addc_u32 s7, s35, s5
	v_mov_b64_e32 v[6:7], s[6:7]
	flat_load_dword v2, v[6:7] sc1
	s_waitcnt vmcnt(0) lgkmcnt(0)
	v_cmp_eq_u32_e32 vcc, v2, v5
	s_and_saveexec_b64 s[4:5], vcc
	s_cbranch_execz .LBB0_627
	s_mov_b32 s22, 1
	s_mov_b64 s[8:9], 0
	s_branch .LBB0_619

; __device__ __forceinline__ unsigned xb_ld(unsigned* p)              { return __hip_atomic_load(p, __ATOMIC_RELAXED, __HIP_MEMORY_SCOPE_AGENT); }
; __device__ __forceinline__ unsigned xb_add(unsigned* p, unsigned v) { return __hip_atomic_fetch_add(p, v, __ATOMIC_RELAXED, __HIP_MEMORY_SCOPE_AGENT); }
; #define XB_SPIN(cond, bar) do { unsigned _sp = 0; while (cond) { __builtin_amdgcn_s_sleep(1); \
;     if ((++_sp & 255u) == 0u) { if (xb_ld(&(bar)[XB_TMO])) break; if (_sp > XB_SPIN_CAP) { atomicAdd(&(bar)[XB_TMO], 1u); break; } } } } while (0)
; __device__ __forceinline__ void xcd_barrier(const XcdBarrier& b) {
;     ...
;     if (threadIdx.x == 0) {
;         unsigned* bar = b.bar;
;         __builtin_amdgcn_s_waitcnt(0);
;         unsigned nloc = b.st[0], nx = b.st[1];
;         if (nloc == 0u) { xcd_barrier_complete(bar, b.x, nloc, nx); b.st[0] = nloc; b.st[1] = nx; }
;         const unsigned old = xb_add(&bar[XB_XSUB(b.x)], 1u);
;         const unsigned gen = old / nloc;
;         if (old + 1u == (gen + 1u) * nloc) {
;             __builtin_amdgcn_fence(__ATOMIC_RELEASE, "agent");
;             asm volatile("s_waitcnt vmcnt(0)" ::: "memory");
;             const unsigned og = xb_add(&bar[XB_TOP], 1u);
;             const unsigned tg = og / nx;
;             if (og + 1u == (tg + 1u) * nx) xb_add(&bar[XB_TOPGEN], 1u);
;             else XB_SPIN(xb_ld(&bar[XB_TOPGEN]) == tg, bar);
;             __builtin_amdgcn_fence(__ATOMIC_ACQUIRE, "agent");
;             xb_add(&bar[XB_XGEN(b.x)], 1u);
;             asm volatile("s_waitcnt vmcnt(0)" ::: "memory");
;         } else {
;             XB_SPIN(xb_ld(&bar[XB_XGEN(b.x)]) == gen, bar);
;             __builtin_amdgcn_fence(__ATOMIC_ACQUIRE, "agent");
;             asm volatile("s_waitcnt vmcnt(0)" ::: "memory");
;         }
.LBB0_845:
	s_lshl_b32 s1, s1, 6
	s_add_i32 s68, s1, 0x500
	s_lshl_b64 s[4:5], s[68:69], 2
	s_add_u32 s4, s40, s4
	s_addc_u32 s5, s41, s5
	v_mov_b64_e32 v[6:7], s[4:5]
	flat_atomic_add v6, v[6:7], v1 sc0
	v_cvt_f32_u32_e32 v5, v4
	v_sub_u32_e32 v7, 0, v4
	v_rcp_iflag_f32_e32 v5, v5
	s_nop 0
	v_mul_f32_e32 v5, 0x4f7ffffe, v5
	v_cvt_u32_f32_e32 v5, v5
	v_mul_lo_u32 v7, v7, v5
	v_mul_hi_u32 v7, v5, v7
	v_add_u32_e32 v5, v5, v7
	s_waitcnt vmcnt(0) lgkmcnt(0)
	v_mul_hi_u32 v5, v6, v5
	v_mul_lo_u32 v7, v5, v4
	v_sub_u32_e32 v7, v6, v7
	v_cmp_ge_u32_e32 vcc, v7, v4
	v_add_u32_e32 v8, 1, v5
	s_nop 0
	v_cndmask_b32_e32 v5, v5, v8, vcc
	v_sub_u32_e32 v8, v7, v4
	v_cndmask_b32_e32 v7, v7, v8, vcc
	v_cmp_ge_u32_e32 vcc, v7, v4
	v_add_u32_e32 v7, 1, v5
	v_add_u32_e32 v8, 1, v6
	v_cndmask_b32_e32 v5, v5, v7, vcc
	v_mad_u64_u32 v[6:7], s[4:5], v4, v5, v[4:5]
	v_cmp_ne_u32_e32 vcc, v8, v6
	s_and_saveexec_b64 s[4:5], vcc
	s_xor_b64 s[4:5], exec, s[4:5]
	s_cbranch_execz .LBB0_858
	s_movk_i32 s68, 0xd40
	s_lshl_b64 s[6:7], s[68:69], 2
	s_add_u32 s8, s40, s6
	s_addc_u32 s9, s41, s7
	v_mov_b64_e32 v[6:7], s[8:9]
	flat_load_dword v2, v[6:7] sc1
	s_waitcnt vmcnt(0) lgkmcnt(0)
	v_cmp_eq_u32_e32 vcc, v2, v5
	s_and_saveexec_b64 s[6:7], vcc
	s_cbranch_execz .LBB0_857
	s_mov_b32 s24, 1
	s_mov_b64 s[10:11], 0
	s_branch .LBB0_849

; __device__ __forceinline__ unsigned xb_ld(unsigned* p)              { return __hip_atomic_load(p, __ATOMIC_RELAXED, __HIP_MEMORY_SCOPE_AGENT); }
; __device__ __forceinline__ unsigned xb_add(unsigned* p, unsigned v) { return __hip_atomic_fetch_add(p, v, __ATOMIC_RELAXED, __HIP_MEMORY_SCOPE_AGENT); }
; #define XB_SPIN(cond, bar) do { unsigned _sp = 0; while (cond) { __builtin_amdgcn_s_sleep(1); \
;     if ((++_sp & 255u) == 0u) { if (xb_ld(&(bar)[XB_TMO])) break; if (_sp > XB_SPIN_CAP) { atomicAdd(&(bar)[XB_TMO], 1u); break; } } } } while (0)
; __device__ __forceinline__ void xcd_barrier(const XcdBarrier& b) {
;     ...
;     if (threadIdx.x == 0) {
;         unsigned* bar = b.bar;
;         __builtin_amdgcn_s_waitcnt(0);
;         unsigned nloc = b.st[0], nx = b.st[1];
;         if (nloc == 0u) { xcd_barrier_complete(bar, b.x, nloc, nx); b.st[0] = nloc; b.st[1] = nx; }
;         const unsigned old = xb_add(&bar[XB_XSUB(b.x)], 1u);
;         const unsigned gen = old / nloc;
;         if (old + 1u == (gen + 1u) * nloc) {
;             __builtin_amdgcn_fence(__ATOMIC_RELEASE, "agent");
;             asm volatile("s_waitcnt vmcnt(0)" ::: "memory");
;             const unsigned og = xb_add(&bar[XB_TOP], 1u);
;             const unsigned tg = og / nx;
;             if (og + 1u == (tg + 1u) * nx) xb_add(&bar[XB_TOPGEN], 1u);
;             else XB_SPIN(xb_ld(&bar[XB_TOPGEN]) == tg, bar);
;             __builtin_amdgcn_fence(__ATOMIC_ACQUIRE, "agent");
;             xb_add(&bar[XB_XGEN(b.x)], 1u);
;             asm volatile("s_waitcnt vmcnt(0)" ::: "memory");
;         } else {
;             XB_SPIN(xb_ld(&bar[XB_XGEN(b.x)]) == gen, bar);
;             __builtin_amdgcn_fence(__ATOMIC_ACQUIRE, "agent");
;             asm volatile("s_waitcnt vmcnt(0)" ::: "memory");
;         }
.LBB0_1043:
	s_lshl_b32 s1, s1, 6
	s_add_i32 s68, s1, 0x500
	s_lshl_b64 s[4:5], s[68:69], 2
	s_add_u32 s4, s38, s4
	s_addc_u32 s5, s39, s5
	v_mov_b64_e32 v[6:7], s[4:5]
	flat_atomic_add v6, v[6:7], v1 sc0
	v_cvt_f32_u32_e32 v5, v4
	v_sub_u32_e32 v7, 0, v4
	v_rcp_iflag_f32_e32 v5, v5
	s_nop 0
	v_mul_f32_e32 v5, 0x4f7ffffe, v5
	v_cvt_u32_f32_e32 v5, v5
	v_mul_lo_u32 v7, v7, v5
	v_mul_hi_u32 v7, v5, v7
	v_add_u32_e32 v5, v5, v7
	s_waitcnt vmcnt(0) lgkmcnt(0)
	v_mul_hi_u32 v5, v6, v5
	v_mul_lo_u32 v7, v5, v4
	v_sub_u32_e32 v7, v6, v7
	v_cmp_ge_u32_e32 vcc, v7, v4
	v_add_u32_e32 v8, 1, v5
	s_nop 0
	v_cndmask_b32_e32 v5, v5, v8, vcc
	v_sub_u32_e32 v8, v7, v4
	v_cndmask_b32_e32 v7, v7, v8, vcc
	v_cmp_ge_u32_e32 vcc, v7, v4
	v_add_u32_e32 v7, 1, v5
	v_add_u32_e32 v8, 1, v6
	v_cndmask_b32_e32 v5, v5, v7, vcc
	v_mad_u64_u32 v[6:7], s[4:5], v4, v5, v[4:5]
	v_cmp_ne_u32_e32 vcc, v8, v6
	s_and_saveexec_b64 s[4:5], vcc
	s_xor_b64 s[4:5], exec, s[4:5]
	s_cbranch_execz .LBB0_1056
	s_movk_i32 s68, 0xd40
	s_lshl_b64 s[6:7], s[68:69], 2
	s_add_u32 s8, s38, s6
	s_addc_u32 s9, s39, s7
	v_mov_b64_e32 v[6:7], s[8:9]
	flat_load_dword v2, v[6:7] sc1
	s_waitcnt vmcnt(0) lgkmcnt(0)
	v_cmp_eq_u32_e32 vcc, v2, v5
	s_and_saveexec_b64 s[6:7], vcc
	s_cbranch_execz .LBB0_1055
	s_mov_b32 s24, 1
	s_mov_b64 s[10:11], 0
	s_branch .LBB0_1047

; __device__ __forceinline__ unsigned xb_ld(unsigned* p)              { return __hip_atomic_load(p, __ATOMIC_RELAXED, __HIP_MEMORY_SCOPE_AGENT); }
; __device__ __forceinline__ unsigned xb_add(unsigned* p, unsigned v) { return __hip_atomic_fetch_add(p, v, __ATOMIC_RELAXED, __HIP_MEMORY_SCOPE_AGENT); }
; #define XB_SPIN(cond, bar) do { unsigned _sp = 0; while (cond) { __builtin_amdgcn_s_sleep(1); \
;     if ((++_sp & 255u) == 0u) { if (xb_ld(&(bar)[XB_TMO])) break; if (_sp > XB_SPIN_CAP) { atomicAdd(&(bar)[XB_TMO], 1u); break; } } } } while (0)
; __device__ __forceinline__ void xcd_barrier(const XcdBarrier& b) {
;     ...
;     if (threadIdx.x == 0) {
;         unsigned* bar = b.bar;
;         __builtin_amdgcn_s_waitcnt(0);
;         unsigned nloc = b.st[0], nx = b.st[1];
;         if (nloc == 0u) { xcd_barrier_complete(bar, b.x, nloc, nx); b.st[0] = nloc; b.st[1] = nx; }
;         const unsigned old = xb_add(&bar[XB_XSUB(b.x)], 1u);
;         const unsigned gen = old / nloc;
;         if (old + 1u == (gen + 1u) * nloc) {
;             __builtin_amdgcn_fence(__ATOMIC_RELEASE, "agent");
;             asm volatile("s_waitcnt vmcnt(0)" ::: "memory");
;             const unsigned og = xb_add(&bar[XB_TOP], 1u);
;             const unsigned tg = og / nx;
;             if (og + 1u == (tg + 1u) * nx) xb_add(&bar[XB_TOPGEN], 1u);
;             else XB_SPIN(xb_ld(&bar[XB_TOPGEN]) == tg, bar);
;             __builtin_amdgcn_fence(__ATOMIC_ACQUIRE, "agent");
;             xb_add(&bar[XB_XGEN(b.x)], 1u);
;             asm volatile("s_waitcnt vmcnt(0)" ::: "memory");
;         } else {
;             XB_SPIN(xb_ld(&bar[XB_XGEN(b.x)]) == gen, bar);
;             __builtin_amdgcn_fence(__ATOMIC_ACQUIRE, "agent");
;             asm volatile("s_waitcnt vmcnt(0)" ::: "memory");
;         }
.LBB0_1774:
	s_lshl_b32 s0, s0, 6
	s_add_i32 s68, s0, 0x500
	s_lshl_b64 s[2:3], s[68:69], 2
	s_add_u32 s2, s34, s2
	s_addc_u32 s3, s35, s3
	v_mov_b64_e32 v[6:7], s[2:3]
	flat_atomic_add v6, v[6:7], v1 sc0
	v_cvt_f32_u32_e32 v5, v4
	v_sub_u32_e32 v7, 0, v4
	v_rcp_iflag_f32_e32 v5, v5
	s_nop 0
	v_mul_f32_e32 v5, 0x4f7ffffe, v5
	v_cvt_u32_f32_e32 v5, v5
	v_mul_lo_u32 v7, v7, v5
	v_mul_hi_u32 v7, v5, v7
	v_add_u32_e32 v5, v5, v7
	s_waitcnt vmcnt(0) lgkmcnt(0)
	v_mul_hi_u32 v5, v6, v5
	v_mul_lo_u32 v7, v5, v4
	v_sub_u32_e32 v7, v6, v7
	v_cmp_ge_u32_e32 vcc, v7, v4
	v_add_u32_e32 v8, 1, v5
	s_nop 0
	v_cndmask_b32_e32 v5, v5, v8, vcc
	v_sub_u32_e32 v8, v7, v4
	v_cndmask_b32_e32 v7, v7, v8, vcc
	v_cmp_ge_u32_e32 vcc, v7, v4
	v_add_u32_e32 v7, 1, v5
	v_add_u32_e32 v8, 1, v6
	v_cndmask_b32_e32 v5, v5, v7, vcc
	v_mad_u64_u32 v[6:7], s[2:3], v4, v5, v[4:5]
	v_cmp_ne_u32_e32 vcc, v8, v6
	s_and_saveexec_b64 s[2:3], vcc
	s_xor_b64 s[2:3], exec, s[2:3]
	s_cbranch_execz .LBB0_1787
	s_movk_i32 s68, 0xd40
	s_lshl_b64 s[4:5], s[68:69], 2
	s_add_u32 s6, s34, s4
	s_addc_u32 s7, s35, s5
	v_mov_b64_e32 v[6:7], s[6:7]
	flat_load_dword v2, v[6:7] sc1
	s_waitcnt vmcnt(0) lgkmcnt(0)
	v_cmp_eq_u32_e32 vcc, v2, v5
	s_and_saveexec_b64 s[4:5], vcc
	s_cbranch_execz .LBB0_1786
	s_mov_b32 s1, 1
	s_mov_b64 s[8:9], 0
	s_branch .LBB0_1778
